# speedup vs baseline: 1.0147x; 1.0047x over previous
.LBB2_1:
	s_mul_i32 s22, s21, 0xe000
	v_add_u32_e32 v196, s22, v214
	v_add_u32_e32 v197, s22, v215
	s_add_u32 s46, s22, s45
	s_add_i32 s21, s21, 1
	s_waitcnt lgkmcnt(0)
	v_mfma_f32_16x16x32_f16 v[130:133], v[22:25], v[42:45], v[130:133]
	ds_read_b128 v[154:157], v196
	v_mfma_f32_16x16x32_f16 v[98:101], v[18:21], v[42:45], v[98:101]
	ds_read_b128 v[158:161], v196 offset:2048
	v_mfma_f32_16x16x32_f16 v[86:89], v[30:33], v[42:45], v[86:89]
	ds_read_b128 v[162:165], v196 offset:4096
	v_mfma_f32_16x16x32_f16 v[74:77], v[26:29], v[42:45], v[74:77]
	ds_read_b128 v[166:169], v196 offset:6144
	v_mfma_f32_16x16x32_f16 v[70:73], v[42:45], v[34:37], v[70:73]
	ds_read_b128 v[170:173], v197 offset:32768
	v_mfma_f32_16x16x32_f16 v[66:69], v[42:45], v[14:17], v[66:69]
	ds_read_b128 v[174:177], v197 offset:34816
	v_mfma_f32_16x16x32_f16 v[62:65], v[22:25], v[38:41], v[62:65]
	ds_read_b128 v[178:181], v197 offset:36864
	v_mfma_f32_16x16x32_f16 v[58:61], v[18:21], v[38:41], v[58:61]
	ds_read_b128 v[182:185], v197 offset:38912
	v_mfma_f32_16x16x32_f16 v[54:57], v[30:33], v[38:41], v[54:57]
	ds_read_b128 v[186:189], v197 offset:40960
	v_mfma_f32_16x16x32_f16 v[50:53], v[26:29], v[38:41], v[50:53]
	ds_read_b128 v[190:193], v197 offset:43008
	v_mfma_f32_16x16x32_f16 v[46:49], v[38:41], v[34:37], v[46:49]
	v_mfma_f32_16x16x32_f16 v[2:5], v[38:41], v[14:17], v[2:5]
	v_mfma_f32_16x16x32_f16 v[78:81], v[22:25], v[10:13], v[78:81]
	v_mfma_f32_16x16x32_f16 v[82:85], v[18:21], v[10:13], v[82:85]
	v_mfma_f32_16x16x32_f16 v[90:93], v[30:33], v[10:13], v[90:93]
	v_mfma_f32_16x16x32_f16 v[94:97], v[26:29], v[10:13], v[94:97]
	v_mfma_f32_16x16x32_f16 v[102:105], v[10:13], v[34:37], v[102:105]
	v_mfma_f32_16x16x32_f16 v[106:109], v[10:13], v[14:17], v[106:109]
	v_mfma_f32_16x16x32_f16 v[110:113], v[22:25], v[6:9], v[110:113]
	v_mfma_f32_16x16x32_f16 v[114:117], v[18:21], v[6:9], v[114:117]
	v_mfma_f32_16x16x32_f16 v[118:121], v[30:33], v[6:9], v[118:121]
	v_mfma_f32_16x16x32_f16 v[122:125], v[26:29], v[6:9], v[122:125]
	v_mfma_f32_16x16x32_f16 v[134:137], v[6:9], v[34:37], v[134:137]
	v_mfma_f32_16x16x32_f16 v[126:129], v[6:9], v[14:17], v[126:129]
	s_cmp_lg_u32 s21, 2
	s_cselect_b32 s21, s21, 0
	s_mul_i32 s22, s21, 0xe000
	v_add_u32_e32 v196, s22, v146
	v_add_u32_e32 v197, s22, v153
	s_waitcnt vmcnt(0) lgkmcnt(0)
	s_barrier
	s_mov_b32 m0, s46
	s_nop 0
	global_load_lds_dwordx4 v194, s[24:25]
	s_add_u32 m0, s46, 0x2000
	s_nop 0
	global_load_lds_dwordx4 v194, s[26:27]
	s_add_u32 m0, s46, 0x4000
	s_nop 0
	global_load_lds_dwordx4 v194, s[28:29]
	s_add_u32 m0, s46, 0x6000
	s_nop 0
	global_load_lds_dwordx4 v194, s[30:31]
	s_add_u32 m0, s46, 0x8000
	s_nop 0
	global_load_lds_dwordx4 v194, s[32:33]
	s_add_u32 m0, s46, 0xa000
	s_nop 0
	global_load_lds_dwordx4 v194, s[34:35]
	s_add_u32 m0, s46, 0xc000
	s_nop 0
	global_load_lds_dwordx4 v194, s[36:37]
	v_add_u32_e32 v194, 0x80, v194
	v_mfma_f32_16x16x32_f16 v[130:133], v[170:173], v[154:157], v[130:133]
	ds_read_b128 v[42:45], v196
	v_mfma_f32_16x16x32_f16 v[98:101], v[174:177], v[154:157], v[98:101]
	ds_read_b128 v[38:41], v196 offset:2048
	v_mfma_f32_16x16x32_f16 v[86:89], v[178:181], v[154:157], v[86:89]
	ds_read_b128 v[10:13], v196 offset:4096
	v_mfma_f32_16x16x32_f16 v[74:77], v[182:185], v[154:157], v[74:77]
	ds_read_b128 v[6:9], v196 offset:6144
	v_mfma_f32_16x16x32_f16 v[70:73], v[154:157], v[186:189], v[70:73]
	ds_read_b128 v[22:25], v197 offset:32768
	v_mfma_f32_16x16x32_f16 v[66:69], v[154:157], v[190:193], v[66:69]
	ds_read_b128 v[18:21], v197 offset:34816
	v_mfma_f32_16x16x32_f16 v[62:65], v[170:173], v[158:161], v[62:65]
	ds_read_b128 v[30:33], v197 offset:36864
	v_mfma_f32_16x16x32_f16 v[58:61], v[174:177], v[158:161], v[58:61]
	ds_read_b128 v[26:29], v197 offset:38912
	v_mfma_f32_16x16x32_f16 v[54:57], v[178:181], v[158:161], v[54:57]
	ds_read_b128 v[34:37], v197 offset:40960
	v_mfma_f32_16x16x32_f16 v[50:53], v[182:185], v[158:161], v[50:53]
	ds_read_b128 v[14:17], v197 offset:43008
	v_mfma_f32_16x16x32_f16 v[46:49], v[158:161], v[186:189], v[46:49]
	v_mfma_f32_16x16x32_f16 v[2:5], v[158:161], v[190:193], v[2:5]
	v_mfma_f32_16x16x32_f16 v[78:81], v[170:173], v[162:165], v[78:81]
	v_mfma_f32_16x16x32_f16 v[82:85], v[174:177], v[162:165], v[82:85]
	v_mfma_f32_16x16x32_f16 v[90:93], v[178:181], v[162:165], v[90:93]
	v_mfma_f32_16x16x32_f16 v[94:97], v[182:185], v[162:165], v[94:97]
	v_mfma_f32_16x16x32_f16 v[102:105], v[162:165], v[186:189], v[102:105]
	v_mfma_f32_16x16x32_f16 v[106:109], v[162:165], v[190:193], v[106:109]
	v_mfma_f32_16x16x32_f16 v[110:113], v[170:173], v[166:169], v[110:113]
	v_mfma_f32_16x16x32_f16 v[114:117], v[174:177], v[166:169], v[114:117]
	v_mfma_f32_16x16x32_f16 v[118:121], v[178:181], v[166:169], v[118:121]
	v_mfma_f32_16x16x32_f16 v[122:125], v[182:185], v[166:169], v[122:125]
	v_mfma_f32_16x16x32_f16 v[134:137], v[166:169], v[186:189], v[134:137]
	v_mfma_f32_16x16x32_f16 v[126:129], v[166:169], v[190:193], v[126:129]
	s_add_u32 s0, s0, 0x80
	s_addc_u32 s1, s1, 0
	s_cmpk_eq_i32 s0, 0x700
	s_cbranch_scc0 .LBB2_1
	s_waitcnt lgkmcnt(0)
	v_mfma_f32_16x16x32_f16 v[130:133], v[22:25], v[42:45], v[130:133]
	ds_read_b128 v[140:143], v214
	ds_read_b128 v[154:157], v214 offset:2048
	v_mfma_f32_16x16x32_f16 v[98:101], v[18:21], v[42:45], v[98:101]
	ds_read_b128 v[158:161], v214 offset:4096
	ds_read_b128 v[162:165], v214 offset:6144
	v_mfma_f32_16x16x32_f16 v[86:89], v[30:33], v[42:45], v[86:89]
	ds_read_b128 v[166:169], v215 offset:32768
	ds_read_b128 v[170:173], v215 offset:34816
	v_mfma_f32_16x16x32_f16 v[74:77], v[26:29], v[42:45], v[74:77]
	ds_read_b128 v[174:177], v215 offset:36864
	ds_read_b128 v[178:181], v215 offset:38912
	v_mfma_f32_16x16x32_f16 v[70:73], v[42:45], v[34:37], v[70:73]
	ds_read_b128 v[182:185], v215 offset:40960
	ds_read_b128 v[186:189], v215 offset:43008
	v_mfma_f32_16x16x32_f16 v[42:45], v[42:45], v[14:17], v[66:69]
	v_mfma_f32_16x16x32_f16 v[62:65], v[22:25], v[38:41], v[62:65]
	v_mfma_f32_16x16x32_f16 v[58:61], v[18:21], v[38:41], v[58:61]
	v_mfma_f32_16x16x32_f16 v[54:57], v[30:33], v[38:41], v[54:57]
	v_mfma_f32_16x16x32_f16 v[50:53], v[26:29], v[38:41], v[50:53]
	v_mfma_f32_16x16x32_f16 v[46:49], v[38:41], v[34:37], v[46:49]
	v_mfma_f32_16x16x32_f16 v[2:5], v[38:41], v[14:17], v[2:5]
	v_mfma_f32_16x16x32_f16 v[38:41], v[22:25], v[10:13], v[78:81]
	v_mfma_f32_16x16x32_f16 v[66:69], v[18:21], v[10:13], v[82:85]
	v_mfma_f32_16x16x32_f16 v[78:81], v[30:33], v[10:13], v[90:93]
	v_mfma_f32_16x16x32_f16 v[82:85], v[26:29], v[10:13], v[94:97]
	v_mfma_f32_16x16x32_f16 v[90:93], v[10:13], v[34:37], v[102:105]
	v_mfma_f32_16x16x32_f16 v[94:97], v[10:13], v[14:17], v[106:109]
	v_mfma_f32_16x16x32_f16 v[22:25], v[22:25], v[6:9], v[110:113]
	v_mfma_f32_16x16x32_f16 v[102:105], v[18:21], v[6:9], v[114:117]
	v_or_b32_e32 v21, v151, v152
	v_and_b32_e32 v20, 63, v0
	v_mfma_f32_16x16x32_f16 v[30:33], v[30:33], v[6:9], v[118:121]
	v_mfma_f32_16x16x32_f16 v[26:29], v[26:29], v[6:9], v[122:125]
	v_mfma_f32_16x16x32_f16 v[34:37], v[6:9], v[34:37], v[134:137]
	v_mfma_f32_16x16x32_f16 v[6:9], v[6:9], v[14:17], v[126:129]
	v_add_u32_e32 v10, 0x16800, v21
	s_waitcnt vmcnt(0) lgkmcnt(0)
	s_waitcnt lgkmcnt(0)
	v_mfma_f32_16x16x32_f16 v[16:19], v[166:169], v[140:143], v[130:133]
	s_barrier
	ds_read_b128 v[106:109], v146 offset:57344
	ds_read_b128 v[110:113], v146 offset:59392
	v_mfma_f32_16x16x32_f16 v[98:101], v[170:173], v[140:143], v[98:101]
	ds_read_b128 v[114:117], v146 offset:61440
	ds_read_b128 v[12:15], v146 offset:63488
	v_add_u32_e32 v0, 0x16000, v21
	v_mfma_f32_16x16x32_f16 v[86:89], v[174:177], v[140:143], v[86:89]
	ds_read_b128 v[122:125], v10
	v_add_u32_e32 v10, 0x17000, v21
	ds_read_b128 v[118:121], v0
	v_mfma_f32_16x16x32_f16 v[74:77], v[178:181], v[140:143], v[74:77]
	ds_read_b128 v[126:129], v10
	v_add_u32_e32 v10, 0x17800, v21
	ds_read_b128 v[130:133], v10
	v_mfma_f32_16x16x32_f16 v[70:73], v[140:143], v[182:185], v[70:73]
	ds_read_b128 v[134:137], v0 offset:8192
	ds_read_b128 v[190:193], v0 offset:10240
	v_mfma_f32_16x16x32_f16 v[42:45], v[140:143], v[186:189], v[42:45]
	v_mfma_f32_16x16x32_f16 v[62:65], v[166:169], v[154:157], v[62:65]
	v_mfma_f32_16x16x32_f16 v[58:61], v[170:173], v[154:157], v[58:61]
	v_mfma_f32_16x16x32_f16 v[54:57], v[174:177], v[154:157], v[54:57]
	v_mfma_f32_16x16x32_f16 v[50:53], v[178:181], v[154:157], v[50:53]
	v_mfma_f32_16x16x32_f16 v[46:49], v[154:157], v[182:185], v[46:49]
	v_mfma_f32_16x16x32_f16 v[140:143], v[154:157], v[186:189], v[2:5]
	v_mfma_f32_16x16x32_f16 v[38:41], v[166:169], v[158:161], v[38:41]
	v_mfma_f32_16x16x32_f16 v[66:69], v[170:173], v[158:161], v[66:69]
	v_mfma_f32_16x16x32_f16 v[78:81], v[174:177], v[158:161], v[78:81]
	v_mfma_f32_16x16x32_f16 v[82:85], v[178:181], v[158:161], v[82:85]
	v_mfma_f32_16x16x32_f16 v[90:93], v[158:161], v[182:185], v[90:93]
	v_mfma_f32_16x16x32_f16 v[94:97], v[158:161], v[186:189], v[94:97]
	v_mfma_f32_16x16x32_f16 v[22:25], v[166:169], v[162:165], v[22:25]
	v_mfma_f32_16x16x32_f16 v[102:105], v[170:173], v[162:165], v[102:105]
	v_mfma_f32_16x16x32_f16 v[30:33], v[174:177], v[162:165], v[30:33]
	v_mfma_f32_16x16x32_f16 v[26:29], v[178:181], v[162:165], v[26:29]
	v_mfma_f32_16x16x32_f16 v[34:37], v[162:165], v[182:185], v[34:37]
	v_mfma_f32_16x16x32_f16 v[152:155], v[162:165], v[186:189], v[6:9]
	s_waitcnt lgkmcnt(0)
	v_mfma_f32_16x16x32_f16 v[156:159], v[118:121], v[106:109], v[16:19]
	s_movk_i32 s0, 0x7c0
	v_add_u32_e32 v216, 0x16000, v215
	ds_read_b128 v[202:205], v216 offset:8192
	ds_read_b128 v[206:209], v216 offset:10240
	v_lshlrev_b32_e32 v16, 6, v144
	v_mov_b32_e32 v17, 0
	v_mov_b32_e32 v139, v17
	v_lshl_add_u64 v[4:5], s[6:7], 0, v[16:17]
	v_lshl_add_u64 v[8:9], v[4:5], 0, v[138:139]
	s_waitcnt vmcnt(0)
	v_lshlrev_b32_e32 v4, 5, v150
	v_lshl_add_u64 v[2:3], s[4:5], 0, v[16:17]
	v_ashrrev_i32_e32 v5, 31, v4
	v_lshl_add_u64 v[2:3], v[2:3], 0, v[138:139]
	v_lshlrev_b64 v[4:5], 2, v[4:5]
	v_lshl_add_u64 v[6:7], v[2:3], 0, v[4:5]
	v_lshl_add_u64 v[4:5], v[8:9], 0, v[4:5]
	v_mfma_f32_16x16x32_f16 v[98:101], v[122:125], v[106:109], v[98:101]
	global_load_dwordx4 v[160:163], v[6:7], off
	v_lshlrev_b32_e32 v18, 5, v147
	v_ashrrev_i32_e32 v19, 31, v18
	v_mfma_f32_16x16x32_f16 v[86:89], v[126:129], v[106:109], v[86:89]
	v_lshlrev_b64 v[18:19], 2, v[18:19]
	ds_read_b128 v[172:175], v214 offset:61440
	ds_read_b128 v[176:179], v214 offset:63488
	v_mfma_f32_16x16x32_f16 v[74:77], v[130:133], v[106:109], v[74:77]
	v_mfma_f32_16x16x32_f16 v[70:73], v[106:109], v[134:137], v[70:73]
	v_mfma_f32_16x16x32_f16 v[42:45], v[106:109], v[190:193], v[42:45]
	global_load_dwordx4 v[106:109], v[4:5], off
	v_lshlrev_b32_e32 v4, 5, v149
	v_ashrrev_i32_e32 v5, 31, v4
	v_lshlrev_b64 v[4:5], 2, v[4:5]
	v_lshl_add_u64 v[6:7], v[2:3], 0, v[4:5]
	v_lshl_add_u64 v[4:5], v[8:9], 0, v[4:5]
	global_load_dwordx4 v[168:171], v[4:5], off
	global_load_dwordx4 v[164:167], v[6:7], off
	v_lshlrev_b32_e32 v4, 5, v148
	v_ashrrev_i32_e32 v5, 31, v4
	v_lshlrev_b64 v[10:11], 2, v[4:5]
	v_lshl_add_u64 v[4:5], v[2:3], 0, v[10:11]
	v_lshl_add_u64 v[10:11], v[8:9], 0, v[10:11]
	global_load_dwordx4 v[210:213], v[10:11], off
	v_lshl_add_u64 v[2:3], v[2:3], 0, v[18:19]
	global_load_dwordx4 v[4:7], v[4:5], off
	v_lshl_add_u64 v[8:9], v[8:9], 0, v[18:19]
	v_add_u32_e32 v18, 0x16000, v215
	v_ashrrev_i32_e32 v10, 7, v145
	ds_read_b128 v[180:183], v18
	v_add_u32_e32 v18, 0x17000, v215
	v_and_b32_e32 v10, -16, v10
	v_add_u32_e32 v19, 0x16800, v215
	ds_read_b128 v[194:197], v18
	v_add_u32_e32 v18, s20, v10
	global_load_dwordx4 v[8:11], v[8:9], off
	ds_read_b128 v[184:187], v19
	v_add_u32_e32 v19, 0x17800, v215
	v_and_or_b32 v21, v145, s0, v1
	global_load_dwordx4 v[0:3], v[2:3], off
	v_mfma_f32_16x16x32_f16 v[62:65], v[118:121], v[110:113], v[62:65]
	ds_read_b128 v[198:201], v19
	v_ashrrev_i32_e32 v19, 31, v18
	ds_read_b128 v[148:151], v214 offset:59392
	v_mfma_f32_16x16x32_f16 v[58:61], v[122:125], v[110:113], v[58:61]
	v_mfma_f32_16x16x32_f16 v[54:57], v[126:129], v[110:113], v[54:57]
	v_mfma_f32_16x16x32_f16 v[50:53], v[130:133], v[110:113], v[50:53]
	v_mfma_f32_16x16x32_f16 v[46:49], v[110:113], v[134:137], v[46:49]
	v_mfma_f32_16x16x32_f16 v[110:113], v[110:113], v[190:193], v[140:143]
	s_nop 2
	ds_read_b128 v[140:143], v214 offset:57344
	v_mfma_f32_16x16x32_f16 v[38:41], v[118:121], v[114:117], v[38:41]
	v_mfma_f32_16x16x32_f16 v[66:69], v[122:125], v[114:117], v[66:69]
	v_mfma_f32_16x16x32_f16 v[78:81], v[126:129], v[114:117], v[78:81]
	v_mfma_f32_16x16x32_f16 v[82:85], v[130:133], v[114:117], v[82:85]
	v_mfma_f32_16x16x32_f16 v[90:93], v[114:117], v[134:137], v[90:93]
	v_mfma_f32_16x16x32_f16 v[94:97], v[114:117], v[190:193], v[94:97]
	s_waitcnt lgkmcnt(0)
	v_mfma_f32_16x16x32_f16 v[114:117], v[180:183], v[140:143], v[156:159]
	v_mfma_f32_16x16x32_f16 v[98:101], v[184:187], v[140:143], v[98:101]
	v_mfma_f32_16x16x32_f16 v[22:25], v[118:121], v[12:15], v[22:25]
	s_waitcnt vmcnt(6)
	s_nop 4
	v_pk_mul_f32 v[120:121], v[114:115], v[106:107] op_sel_hi:[1,0]
	v_lshlrev_b64 v[118:119], 17, v[18:19]
	v_lshl_or_b32 v118, v21, 6, v118
	v_mfma_f32_16x16x32_f16 v[102:105], v[122:125], v[12:15], v[102:105]
	v_mul_f32_e64 v122, v116, v107
	v_mul_f32_e64 v123, v117, v107
	v_pk_fma_f32 v[124:125], v[114:115], v[160:161], v[120:121] op_sel:[0,0,1] op_sel_hi:[1,1,0] neg_lo:[0,0,1] neg_hi:[0,0,1]
	v_pk_fma_f32 v[114:115], v[114:115], v[160:161], v[120:121] op_sel:[0,0,1] op_sel_hi:[1,0,0]
	v_pk_fma_f32 v[120:121], v[116:117], v[160:161], v[122:123] op_sel:[0,1,1] op_sel_hi:[1,1,0] neg_lo:[0,0,1] neg_hi:[0,0,1]
	v_pk_fma_f32 v[116:117], v[116:117], v[160:161], v[122:123] op_sel:[0,1,1] op_sel_hi:[1,1,0]
	v_cvt_pk_f16_f32 v114, v124, v115
	v_cvt_pk_f16_f32 v115, v120, v117
	v_pk_mul_f32 v[116:117], v[98:99], v[108:109] op_sel_hi:[1,0]
	v_mov_b32_e32 v122, v163
	v_pk_fma_f32 v[120:121], v[98:99], v[162:163], v[116:117] op_sel:[0,0,1] op_sel_hi:[1,1,0] neg_lo:[0,0,1] neg_hi:[0,0,1]
	v_pk_fma_f32 v[98:99], v[98:99], v[162:163], v[116:117] op_sel:[0,0,1] op_sel_hi:[1,0,0]
	v_mfma_f32_16x16x32_f16 v[30:33], v[126:129], v[12:15], v[30:33]
	v_cvt_pk_f16_f32 v116, v120, v99
	v_mov_b32_e32 v120, v109
	v_pk_mul_f32 v[98:99], v[100:101], v[120:121] op_sel_hi:[1,0]
	v_mfma_f32_16x16x32_f16 v[26:29], v[130:133], v[12:15], v[26:29]
	v_fma_f32 v124, v100, v122, -v99
	v_fma_f32 v125, v101, v122, -v98
	v_pk_fma_f32 v[98:99], v[100:101], v[122:123], v[98:99] op_sel:[0,0,1] op_sel_hi:[1,0,0]
	s_nop 0
	v_cvt_pk_f16_f32 v117, v124, v99
	v_lshlrev_b64 v[124:125], 1, v[118:119]
	v_lshl_add_u64 v[126:127], s[10:11], 0, v[124:125]
	v_mfma_f32_16x16x32_f16 v[34:37], v[12:15], v[134:137], v[34:37]
	v_mfma_f32_16x16x32_f16 v[98:101], v[12:15], v[190:193], v[152:155]
	v_lshl_add_u64 v[12:13], v[126:127], 0, v[16:17]
	v_lshl_add_u64 v[126:127], v[12:13], 0, v[138:139]
	global_store_dwordx4 v[126:127], v[114:117], off sc1
	v_mfma_f32_16x16x32_f16 v[12:15], v[194:197], v[140:143], v[86:89]
	v_mfma_f32_16x16x32_f16 v[74:77], v[198:201], v[140:143], v[74:77]
	v_mfma_f32_16x16x32_f16 v[58:61], v[184:187], v[148:151], v[58:61]
	s_nop 5
	v_mul_f32_e64 v86, v12, v106
	v_mul_f32_e64 v87, v13, v106
	v_pk_fma_f32 v[88:89], v[12:13], v[160:161], v[86:87] op_sel:[0,0,1] op_sel_hi:[1,1,0] neg_lo:[0,0,1] neg_hi:[0,0,1]
	v_pk_fma_f32 v[12:13], v[12:13], v[160:161], v[86:87] op_sel:[0,0,1] op_sel_hi:[1,0,0]
	v_mfma_f32_16x16x32_f16 v[54:57], v[194:197], v[148:151], v[54:57]
	v_cvt_pk_f16_f32 v86, v88, v13
	v_pk_mul_f32 v[12:13], v[14:15], v[106:107] op_sel:[0,1]
	s_nop 0
	v_pk_fma_f32 v[88:89], v[14:15], v[160:161], v[12:13] op_sel:[0,1,1] op_sel_hi:[1,1,0] neg_lo:[0,0,1] neg_hi:[0,0,1]
	v_pk_fma_f32 v[12:13], v[14:15], v[160:161], v[12:13] op_sel:[0,1,1] op_sel_hi:[1,1,0]
	v_mfma_f32_16x16x32_f16 v[50:53], v[198:201], v[148:151], v[50:53]
	v_cvt_pk_f16_f32 v87, v88, v13
	v_pk_mul_f32 v[88:89], v[74:75], v[108:109] op_sel_hi:[1,0]
	v_mfma_f32_16x16x32_f16 v[12:15], v[140:143], v[206:209], v[42:45]
	s_nop 2
	v_fma_f32 v42, v74, v162, -v89
	v_fma_f32 v43, v75, v163, -v88
	v_pk_fma_f32 v[44:45], v[74:75], v[162:163], v[88:89] op_sel:[0,0,1] op_sel_hi:[1,0,0]
	v_mfma_f32_16x16x32_f16 v[38:41], v[180:183], v[172:175], v[38:41]
	v_cvt_pk_f16_f32 v88, v42, v45
	v_mfma_f32_16x16x32_f16 v[42:45], v[180:183], v[148:151], v[62:65]
	s_nop 2
	v_mul_f32_e64 v62, v76, v120
	v_mul_f32_e64 v63, v77, v120
	v_mfma_f32_16x16x32_f16 v[66:69], v[184:187], v[172:175], v[66:69]
	v_fma_f32 v64, v76, v122, -v63
	v_fma_f32 v65, v77, v122, -v62
	v_pk_fma_f32 v[62:63], v[76:77], v[122:123], v[62:63] op_sel:[0,0,1] op_sel_hi:[1,0,0]
	s_nop 0
	v_cvt_pk_f16_f32 v89, v64, v63
	v_lshl_add_u64 v[62:63], s[12:13], 0, v[124:125]
	v_lshl_add_u64 v[62:63], v[62:63], 0, v[16:17]
	v_lshl_add_u64 v[106:107], v[62:63], 0, v[138:139]
	s_waitcnt vmcnt(6)
	v_pk_mul_f32 v[62:63], v[42:43], v[168:169] op_sel_hi:[1,0]
	global_store_dwordx4 v[106:107], v[86:89], off sc1
	s_waitcnt vmcnt(6)
	v_pk_fma_f32 v[64:65], v[42:43], v[164:165], v[62:63] op_sel:[0,0,1] op_sel_hi:[1,1,0] neg_lo:[0,0,1] neg_hi:[0,0,1]
	v_pk_fma_f32 v[42:43], v[42:43], v[164:165], v[62:63] op_sel:[0,0,1] op_sel_hi:[1,0,0]
	v_pk_mul_f32 v[62:63], v[44:45], v[168:169] op_sel:[0,1]
	v_cvt_pk_f16_f32 v42, v64, v43
	v_pk_fma_f32 v[74:75], v[44:45], v[164:165], v[62:63] op_sel:[0,1,1] op_sel_hi:[1,1,0] neg_lo:[0,0,1] neg_hi:[0,0,1]
	v_pk_fma_f32 v[44:45], v[44:45], v[164:165], v[62:63] op_sel:[0,1,1] op_sel_hi:[1,1,0]
	v_mov_b32_e32 v86, v171
	v_cvt_pk_f16_f32 v43, v74, v45
	v_pk_mul_f32 v[44:45], v[58:59], v[170:171] op_sel_hi:[1,0]
	v_mov_b32_e32 v88, v167
	v_pk_fma_f32 v[74:75], v[58:59], v[166:167], v[44:45] op_sel:[0,0,1] op_sel_hi:[1,1,0] neg_lo:[0,0,1] neg_hi:[0,0,1]
	v_pk_fma_f32 v[44:45], v[58:59], v[166:167], v[44:45] op_sel:[0,0,1] op_sel_hi:[1,0,0]
	v_pk_mul_f32 v[58:59], v[60:61], v[86:87] op_sel_hi:[1,0]
	v_cvt_pk_f16_f32 v44, v74, v45
	v_pk_fma_f32 v[108:109], v[60:61], v[88:89], v[58:59] op_sel:[0,0,1] op_sel_hi:[1,0,0] neg_lo:[0,0,1] neg_hi:[0,0,1]
	v_pk_fma_f32 v[58:59], v[60:61], v[88:89], v[58:59] op_sel:[0,0,1] op_sel_hi:[1,0,0]
	v_mfma_f32_16x16x32_f16 v[74:77], v[194:197], v[172:175], v[78:81]
	v_cvt_pk_f16_f32 v45, v108, v59
	global_store_dwordx4 v[126:127], v[42:45], off offset:2048 sc1
	v_pk_mul_f32 v[58:59], v[54:55], v[168:169] op_sel_hi:[1,0]
	v_mfma_f32_16x16x32_f16 v[22:25], v[180:183], v[176:179], v[22:25]
	v_fma_f32 v78, v54, v164, -v59
	v_fma_f32 v79, v55, v165, -v58
	v_pk_fma_f32 v[54:55], v[54:55], v[164:165], v[58:59] op_sel:[0,0,1] op_sel_hi:[1,0,0]
	v_mfma_f32_16x16x32_f16 v[42:45], v[198:201], v[172:175], v[82:85]
	v_cvt_pk_f16_f32 v54, v78, v55
	s_nop 1
	v_pk_mul_f32 v[82:83], v[56:57], v[168:169] op_sel:[0,1]
	v_mfma_f32_16x16x32_f16 v[30:33], v[194:197], v[176:179], v[30:33]
	v_fma_f32 v84, v56, v165, -v83
	v_fma_f32 v85, v57, v165, -v82
	v_pk_fma_f32 v[56:57], v[56:57], v[164:165], v[82:83] op_sel:[0,1,1] op_sel_hi:[1,1,0]
	s_nop 0
	v_cvt_pk_f16_f32 v55, v84, v57
	v_pk_mul_f32 v[56:57], v[50:51], v[170:171] op_sel_hi:[1,0]
	v_mfma_f32_16x16x32_f16 v[26:29], v[198:201], v[176:179], v[26:29]
	v_fma_f32 v82, v50, v166, -v57
	v_fma_f32 v83, v51, v167, -v56
	v_pk_fma_f32 v[50:51], v[50:51], v[166:167], v[56:57] op_sel:[0,0,1] op_sel_hi:[1,0,0]
	s_nop 0
	v_cvt_pk_f16_f32 v56, v82, v51
	v_pk_mul_f32 v[50:51], v[52:53], v[86:87] op_sel_hi:[1,0]
	v_mfma_f32_16x16x32_f16 v[82:85], v[184:187], v[176:179], v[102:105]
	v_fma_f32 v86, v52, v88, -v51
	v_fma_f32 v87, v53, v88, -v50
	v_pk_fma_f32 v[50:51], v[52:53], v[88:89], v[50:51] op_sel:[0,0,1] op_sel_hi:[1,0,0]
	s_nop 0
	v_cvt_pk_f16_f32 v57, v86, v51
	global_store_dwordx4 v[106:107], v[54:57], off offset:2048 sc1
	s_waitcnt vmcnt(7)
	v_pk_mul_f32 v[50:51], v[38:39], v[210:211] op_sel_hi:[1,0]
	v_mfma_f32_16x16x32_f16 v[70:73], v[140:143], v[202:205], v[70:73]
	v_mul_f32_e64 v56, v40, v211
	v_mul_f32_e64 v57, v41, v211
	s_waitcnt vmcnt(6)
	v_pk_fma_f32 v[52:53], v[38:39], v[4:5], v[50:51] op_sel:[0,0,1] op_sel_hi:[1,1,0] neg_lo:[0,0,1] neg_hi:[0,0,1]
	v_pk_fma_f32 v[38:39], v[38:39], v[4:5], v[50:51] op_sel:[0,0,1] op_sel_hi:[1,0,0]
	v_pk_fma_f32 v[86:87], v[40:41], v[4:5], v[56:57] op_sel:[0,1,1] op_sel_hi:[1,1,0] neg_lo:[0,0,1] neg_hi:[0,0,1]
	v_pk_fma_f32 v[40:41], v[40:41], v[4:5], v[56:57] op_sel:[0,1,1] op_sel_hi:[1,1,0]
	v_cvt_pk_f16_f32 v38, v52, v39
	v_cvt_pk_f16_f32 v39, v86, v41
	v_pk_mul_f32 v[40:41], v[66:67], v[212:213] op_sel_hi:[1,0]
	v_or_b32_e32 v54, 0x800, v118
	v_pk_fma_f32 v[56:57], v[66:67], v[6:7], v[40:41] op_sel:[0,0,1] op_sel_hi:[1,1,0] neg_lo:[0,0,1] neg_hi:[0,0,1]
	v_pk_fma_f32 v[40:41], v[66:67], v[6:7], v[40:41] op_sel:[0,0,1] op_sel_hi:[1,0,0]
	v_mov_b32_e32 v55, v119
	v_cvt_pk_f16_f32 v40, v56, v41
	v_mov_b32_e32 v56, v213
	v_pk_mul_f32 v[66:67], v[68:69], v[56:57] op_sel_hi:[1,0]
	v_mov_b32_e32 v86, v7
	v_pk_fma_f32 v[88:89], v[68:69], v[86:87], v[66:67] op_sel:[0,0,1] op_sel_hi:[1,0,0] neg_lo:[0,0,1] neg_hi:[0,0,1]
	v_pk_fma_f32 v[66:67], v[68:69], v[86:87], v[66:67] op_sel:[0,0,1] op_sel_hi:[1,0,0]
	v_lshlrev_b64 v[54:55], 1, v[54:55]
	v_cvt_pk_f16_f32 v41, v88, v67
	v_lshl_add_u64 v[66:67], s[10:11], 0, v[54:55]
	v_lshl_add_u64 v[66:67], v[66:67], 0, v[16:17]
	v_lshl_add_u64 v[66:67], v[66:67], 0, v[138:139]
	global_store_dwordx4 v[66:67], v[38:41], off sc1
	v_or_b32_e32 v118, 0xc00, v118
	v_mfma_f32_16x16x32_f16 v[46:49], v[148:151], v[202:205], v[46:49]
	v_mul_f32_e64 v38, v74, v210
	v_mul_f32_e64 v39, v75, v210
	v_pk_fma_f32 v[40:41], v[74:75], v[4:5], v[38:39] op_sel:[0,0,1] op_sel_hi:[1,1,0] neg_lo:[0,0,1] neg_hi:[0,0,1]
	v_pk_fma_f32 v[38:39], v[74:75], v[4:5], v[38:39] op_sel:[0,0,1] op_sel_hi:[1,0,0]
	v_mfma_f32_16x16x32_f16 v[58:61], v[172:175], v[202:205], v[90:93]
	v_cvt_pk_f16_f32 v38, v40, v39
	v_pk_mul_f32 v[40:41], v[76:77], v[210:211] op_sel:[0,1]
	s_nop 0
	v_pk_fma_f32 v[66:67], v[76:77], v[4:5], v[40:41] op_sel:[0,1,1] op_sel_hi:[1,1,0] neg_lo:[0,0,1] neg_hi:[0,0,1]
	v_pk_fma_f32 v[4:5], v[76:77], v[4:5], v[40:41] op_sel:[0,1,1] op_sel_hi:[1,1,0]
	v_mfma_f32_16x16x32_f16 v[34:37], v[176:179], v[202:205], v[34:37]
	v_cvt_pk_f16_f32 v39, v66, v5
	v_pk_mul_f32 v[4:5], v[42:43], v[212:213] op_sel_hi:[1,0]
	s_nop 0
	v_pk_fma_f32 v[40:41], v[42:43], v[6:7], v[4:5] op_sel:[0,0,1] op_sel_hi:[1,1,0] neg_lo:[0,0,1] neg_hi:[0,0,1]
	v_pk_fma_f32 v[4:5], v[42:43], v[6:7], v[4:5] op_sel:[0,0,1] op_sel_hi:[1,0,0]
	v_mfma_f32_16x16x32_f16 v[62:65], v[148:151], v[206:209], v[110:113]
	v_cvt_pk_f16_f32 v40, v40, v5
	v_pk_mul_f32 v[4:5], v[44:45], v[56:57] op_sel_hi:[1,0]
	s_nop 0
	v_pk_fma_f32 v[6:7], v[44:45], v[86:87], v[4:5] op_sel:[0,0,1] op_sel_hi:[1,0,0] neg_lo:[0,0,1] neg_hi:[0,0,1]
	v_pk_fma_f32 v[4:5], v[44:45], v[86:87], v[4:5] op_sel:[0,0,1] op_sel_hi:[1,0,0]
	v_mfma_f32_16x16x32_f16 v[78:81], v[172:175], v[206:209], v[94:97]
	v_cvt_pk_f16_f32 v41, v6, v5
	v_lshl_add_u64 v[4:5], s[12:13], 0, v[54:55]
	v_lshl_add_u64 v[4:5], v[4:5], 0, v[16:17]
	v_lshl_add_u64 v[4:5], v[4:5], 0, v[138:139]
	global_store_dwordx4 v[4:5], v[38:41], off sc1
	s_waitcnt vmcnt(7)
	v_pk_mul_f32 v[4:5], v[22:23], v[8:9] op_sel_hi:[1,0]
	v_mfma_f32_16x16x32_f16 v[50:53], v[176:179], v[206:209], v[98:101]
	s_waitcnt vmcnt(6)
	v_pk_fma_f32 v[6:7], v[22:23], v[0:1], v[4:5] op_sel:[0,0,1] op_sel_hi:[1,1,0] neg_lo:[0,0,1] neg_hi:[0,0,1]
	v_pk_fma_f32 v[4:5], v[22:23], v[0:1], v[4:5] op_sel:[0,0,1] op_sel_hi:[1,0,0]
	v_mov_b32_e32 v38, v3
	v_cvt_pk_f16_f32 v4, v6, v5
	v_pk_mul_f32 v[6:7], v[24:25], v[8:9] op_sel:[0,1]
	s_nop 0
	v_pk_fma_f32 v[22:23], v[24:25], v[0:1], v[6:7] op_sel:[0,1,1] op_sel_hi:[1,1,0] neg_lo:[0,0,1] neg_hi:[0,0,1]
	v_pk_fma_f32 v[6:7], v[24:25], v[0:1], v[6:7] op_sel:[0,1,1] op_sel_hi:[1,1,0]
	s_nop 0
	v_cvt_pk_f16_f32 v5, v22, v7
	v_pk_mul_f32 v[6:7], v[82:83], v[10:11] op_sel_hi:[1,0]
	s_nop 0
	v_pk_fma_f32 v[22:23], v[82:83], v[2:3], v[6:7] op_sel:[0,0,1] op_sel_hi:[1,1,0] neg_lo:[0,0,1] neg_hi:[0,0,1]
	v_pk_fma_f32 v[6:7], v[82:83], v[2:3], v[6:7] op_sel:[0,0,1] op_sel_hi:[1,0,0]
	s_nop 0
	v_cvt_pk_f16_f32 v6, v22, v7
	v_mov_b32_e32 v22, v11
	v_pk_mul_f32 v[24:25], v[84:85], v[22:23] op_sel_hi:[1,0]
	s_nop 0
	v_pk_fma_f32 v[40:41], v[84:85], v[38:39], v[24:25] op_sel:[0,0,1] op_sel_hi:[1,0,0] neg_lo:[0,0,1] neg_hi:[0,0,1]
	v_pk_fma_f32 v[24:25], v[84:85], v[38:39], v[24:25] op_sel:[0,0,1] op_sel_hi:[1,0,0]
	s_nop 0
	v_cvt_pk_f16_f32 v7, v40, v25
	v_lshlrev_b64 v[24:25], 1, v[118:119]
	v_lshl_add_u64 v[40:41], s[10:11], 0, v[24:25]
	v_lshl_add_u64 v[40:41], v[40:41], 0, v[16:17]
	v_lshl_add_u64 v[40:41], v[40:41], 0, v[138:139]
	global_store_dwordx4 v[40:41], v[4:7], off sc1
	s_nop 1
	v_pk_mul_f32 v[4:5], v[30:31], v[8:9] op_sel_hi:[1,0]
	s_nop 0
	v_pk_fma_f32 v[6:7], v[30:31], v[0:1], v[4:5] op_sel:[0,0,1] op_sel_hi:[1,1,0] neg_lo:[0,0,1] neg_hi:[0,0,1]
	v_pk_fma_f32 v[4:5], v[30:31], v[0:1], v[4:5] op_sel:[0,0,1] op_sel_hi:[1,0,0]
	s_nop 0
	v_cvt_pk_f16_f32 v4, v6, v5
	v_pk_mul_f32 v[6:7], v[32:33], v[8:9] op_sel:[0,1]
	s_nop 0
	v_pk_fma_f32 v[8:9], v[32:33], v[0:1], v[6:7] op_sel:[0,1,1] op_sel_hi:[1,1,0] neg_lo:[0,0,1] neg_hi:[0,0,1]
	v_pk_fma_f32 v[0:1], v[32:33], v[0:1], v[6:7] op_sel:[0,1,1] op_sel_hi:[1,1,0]
	s_nop 0
	v_cvt_pk_f16_f32 v5, v8, v1
	v_pk_mul_f32 v[0:1], v[26:27], v[10:11] op_sel_hi:[1,0]
	s_nop 0
	v_pk_fma_f32 v[6:7], v[26:27], v[2:3], v[0:1] op_sel:[0,0,1] op_sel_hi:[1,1,0] neg_lo:[0,0,1] neg_hi:[0,0,1]
	v_pk_fma_f32 v[0:1], v[26:27], v[2:3], v[0:1] op_sel:[0,0,1] op_sel_hi:[1,0,0]
	s_nop 0
	v_cvt_pk_f16_f32 v6, v6, v1
	v_pk_mul_f32 v[0:1], v[28:29], v[22:23] op_sel_hi:[1,0]
	s_nop 0
	v_pk_fma_f32 v[2:3], v[28:29], v[38:39], v[0:1] op_sel:[0,0,1] op_sel_hi:[1,0,0] neg_lo:[0,0,1] neg_hi:[0,0,1]
	v_pk_fma_f32 v[0:1], v[28:29], v[38:39], v[0:1] op_sel:[0,0,1] op_sel_hi:[1,0,0]
	v_cvt_pk_f16_f32 v3, v48, v49
	v_cvt_pk_f16_f32 v7, v2, v1
	v_lshl_add_u64 v[0:1], s[12:13], 0, v[24:25]
	v_lshl_add_u64 v[0:1], v[0:1], 0, v[16:17]
	v_lshl_add_u64 v[0:1], v[0:1], 0, v[138:139]
	global_store_dwordx4 v[0:1], v[4:7], off sc1
	v_lshlrev_b64 v[0:1], 18, v[18:19]
	v_lshlrev_b32_e32 v2, 7, v145
	v_lshl_add_u64 v[0:1], s[14:15], 0, v[0:1]
	v_and_b32_e32 v16, 0x3e000, v2
	v_lshl_add_u64 v[0:1], v[0:1], 0, v[16:17]
	v_lshlrev_b32_e32 v16, 4, v20
	v_lshl_add_u64 v[4:5], v[0:1], 0, v[16:17]
	v_lshlrev_b32_e32 v16, 12, v144
	v_cvt_pk_f16_f32 v2, v46, v47
	v_cvt_pk_f16_f32 v1, v72, v73
	v_cvt_pk_f16_f32 v0, v70, v71
	v_lshl_add_u64 v[4:5], v[4:5], 0, v[16:17]
	global_store_dwordx4 v[4:5], v[0:3], off sc1
	s_nop 1
	v_cvt_pk_f16_f32 v3, v36, v37
	v_cvt_pk_f16_f32 v2, v34, v35
	v_cvt_pk_f16_f32 v1, v60, v61
	v_cvt_pk_f16_f32 v0, v58, v59
	global_store_dwordx4 v[4:5], v[0:3], off offset:1024 sc1
	s_nop 1
	v_cvt_pk_f16_f32 v3, v64, v65
	v_cvt_pk_f16_f32 v2, v62, v63
	v_cvt_pk_f16_f32 v1, v14, v15
	v_cvt_pk_f16_f32 v0, v12, v13
	global_store_dwordx4 v[4:5], v[0:3], off offset:2048 sc1
	s_nop 1
	v_cvt_pk_f16_f32 v3, v52, v53
	v_cvt_pk_f16_f32 v2, v50, v51
	v_cvt_pk_f16_f32 v1, v80, v81
	v_cvt_pk_f16_f32 v0, v78, v79
	global_store_dwordx4 v[4:5], v[0:3], off offset:3072 sc1
	s_endpgm
	.p2align	8
